# NA unit loop: the previous unit's output stores are no longer drained (vmcnt(0)) before the next unit starts
# speedup vs baseline: 1.0030x; 1.0030x over previous
; #define LAS __attribute__((address_space(3)))
; __device__ __forceinline__ void na_fast_unit(int unit, const bf16_t* P, const float* rpb, bf16_t* AO, LAS unsigned char* lds) {
;     const int tid = threadIdx.x, lane = tid & 63, wv = __builtin_amdgcn_readfirstlane(tid >> 6);
;     const int cq = wv & 3, kh = wv >> 2;
;     const int r = unit & 63, h = (unit >> 6) & 7, b = unit >> 9;
;     const int l15 = lane & 15, q = lane >> 4, trq = l15 >> 2, trp = lane & 3;
;     const int rstart = min(max(r - 4, 0), 56);
;     const int col = 16 * cq + l15, cstart = min(max(col - 8, 0), 48);
;     const int ct0 = min(max(cq - 1, 0), 1);
;     const float scale = 0.08838834764831845f;
; __global__ void __launch_bounds__(512, 2) mk_fwd(Args a) {
;     ...
;         unsigned* qctr = (unsigned*)(ws + WS_CTL) + 8192 + 64 * rep;
;         for (;;) {
;             __syncthreads();
;             if (tid == 0) *(volatile LAS unsigned*)(lds + LDS_BARW + 32) = atomicAdd(qctr, 1u);
;             __syncthreads();
;             const unsigned u = *(volatile LAS unsigned*)(lds + LDS_BARW + 32);
;             if (u >= (unsigned)(NB * 8 * 64)) break;
;             na_fast_unit((int)u, Pb, a.in[I_RPB], AO, lds);
.LBB0_1206:
	v_or_b32_e32 v3, 0x600, v0
	s_add_u32 s8, s94, 0x8000
	v_and_b32_e32 v2, 0x78, v181
	v_or_b32_e32 v104, 64, v168
	v_lshrrev_b32_e32 v105, 4, v3
	v_readlane_b32 s6, v255, 3
	s_addc_u32 s9, s95, 0
	v_bfe_u32 v106, v3, 4, 6
	v_mul_u32_u24_e32 v107, 0x110, v168
	v_mul_u32_u24_e32 v108, 0x110, v170
	v_mul_u32_u24_e32 v109, 0x120, v104
	v_mul_u32_u24_e32 v110, 0x110, v105
	v_mul_u32_u24_e32 v111, 0x120, v105
	s_add_i32 s2, 0, 0x11800
	s_add_i32 s3, 0, 0x1a000
	v_lshlrev_b32_e32 v114, 11, v86
	v_lshl_add_u32 v115, v1, 2, 0
	v_lshlrev_b32_e32 v86, 1, v1
	v_readlane_b32 s7, v255, 4
	v_mov_b32_e32 v3, 0x200
	s_add_i32 s45, 0, 0x23fe0
	v_lshlrev_b32_e32 v92, 1, v2
	v_mbcnt_lo_u32_b32 v2, -1, 0
	v_cmp_eq_u32_e64 s[4:5], 0, v0
	s_movk_i32 s13, 0x110
	v_add_u32_e32 v112, s2, v176
	v_add_u32_e32 v113, s3, v178
	v_add_u32_e32 v116, v115, v114
	v_lshl_add_u64 v[88:89], s[6:7], 0, v[86:87]
	v_lshl_or_b32 v117, v169, 9, v3
	v_lshlrev_b32_e32 v118, 9, v180
	v_lshlrev_b32_e32 v119, 9, v179
	v_add_u32_e32 v120, 0, v176
	v_add_u32_e32 v121, 0, v178
	v_add_u32_e32 v122, s2, v177
	v_add_u32_e32 v123, s3, v177
	v_lshl_add_u32 v124, v169, 2, 0
	v_mov_b32_e32 v125, s45
	s_movk_i32 s46, 0x3200
	s_mov_b64 s[10:11], 0x1400
	s_movk_i32 s47, 0x1000
	v_add_u32_e32 v126, v174, v107
	v_add_u32_e32 v127, v174, v171
	v_add_u32_e32 v128, v174, v108
	v_add_u32_e32 v129, v174, v172
	v_add_u32_e32 v130, v174, v109
	v_add_u32_e32 v131, v174, v110
	v_add_u32_e32 v132, v174, v111
	s_mov_b32 s12, 0x3db504f3
	v_lshlrev_b32_e32 v90, 1, v175
	v_mbcnt_hi_u32_b32 v133, -1, v2
	s_and_saveexec_b64 s[2:3], s[4:5]
	v_mov_b32_e32 v3, 1
	global_atomic_add v253, v87, v3, s[8:9] sc0
	s_waitcnt vmcnt(0)
	s_mov_b64 exec, s[2:3]
	s_branch .LBB0_1209

; #define LAS __attribute__((address_space(3)))
; __global__ void __launch_bounds__(512, 2) mk_fwd(Args a) {
;     ...
;         for (;;) {
;             __syncthreads();
;             if (tid == 0) *(volatile LAS unsigned*)(lds + LDS_BARW + 32) = atomicAdd(qctr, 1u);
;             __syncthreads();
;             const unsigned u = *(volatile LAS unsigned*)(lds + LDS_BARW + 32);
;             if (u >= (unsigned)(NB * 8 * 64)) break;
.LBB0_1209:
	s_waitcnt lgkmcnt(0)
	s_barrier
	s_and_saveexec_b64 s[2:3], s[4:5]
	s_cbranch_execz .LBB0_1213
	v_mov_b32_e32 v3, s45
	ds_write_b32 v3, v253
	v_mov_b32_e32 v2, 1
	s_nop 0
	global_atomic_add v253, v87, v2, s[8:9] sc0
